# v40
# baseline (speedup 1.0000x reference)
.LBB3_61:
	v_lshrrev_b32_e32 v67, 5, v66
	v_lshlrev_b32_e32 v88, 8, v72
	s_waitcnt vmcnt(8)
	v_xor_b32_e32 v2, v67, v71
	v_lshl_or_b32 v80, v2, 4, v88
	s_waitcnt lgkmcnt(0)
	s_barrier
	ds_read_b128 v[2:5], v80
	v_or_b32_e32 v6, 32, v72
	v_min_i32_e32 v72, 59, v6
	v_lshlrev_b32_e32 v89, 8, v72
	v_bitop3_b32 v6, v67, v72, 15 bitop3:0x78
	v_lshl_or_b32 v81, v6, 4, v89
	s_waitcnt vmcnt(7) lgkmcnt(0)
	v_mfma_f32_32x32x16_f16 v[18:33], v[2:5], v[46:49], 0
	ds_read_b128 v[2:5], v81
	v_and_b32_e32 v90, 15, v72
	v_bitop3_b32 v72, v67, v90, 2 bitop3:0x36
	v_lshl_or_b32 v79, v72, 4, v89
	s_mov_b32 s0, 0x9000
	s_waitcnt lgkmcnt(0)
	v_mfma_f32_32x32x16_f16 v[2:17], v[2:5], v[46:49], 0
	v_bitop3_b32 v46, v67, v71, 2 bitop3:0x36
	v_lshl_or_b32 v78, v46, 4, v88
	ds_read_b128 v[46:49], v78
	s_waitcnt vmcnt(6) lgkmcnt(0)
	v_mfma_f32_32x32x16_f16 v[18:33], v[46:49], v[34:37], v[18:33]
	ds_read_b128 v[46:49], v79
	s_waitcnt lgkmcnt(0)
	v_mfma_f32_32x32x16_f16 v[2:17], v[46:49], v[34:37], v[2:17]
	v_bitop3_b32 v34, v67, v71, 4 bitop3:0x36
	v_lshl_or_b32 v77, v34, 4, v88
	ds_read_b128 v[34:37], v77
	v_bitop3_b32 v46, v67, v90, 4 bitop3:0x36
	v_lshl_or_b32 v76, v46, 4, v89
	v_bitop3_b32 v46, v67, v90, 6 bitop3:0x36
	v_lshl_or_b32 v75, v46, 4, v89
	s_waitcnt vmcnt(5) lgkmcnt(0)
	v_mfma_f32_32x32x16_f16 v[18:33], v[34:37], v[54:57], v[18:33]
	ds_read_b128 v[34:37], v76
	v_bitop3_b32 v46, v67, v71, 8 bitop3:0x36
	v_lshl_or_b32 v72, v46, 4, v88
	s_waitcnt lgkmcnt(0)
	v_mfma_f32_32x32x16_f16 v[2:17], v[34:37], v[54:57], v[2:17]
	v_bitop3_b32 v34, v67, v71, 6 bitop3:0x36
	v_lshl_or_b32 v74, v34, 4, v88
	ds_read_b128 v[34:37], v74
	ds_read_b128 v[54:57], v72
	s_waitcnt vmcnt(4) lgkmcnt(1)
	v_mfma_f32_32x32x16_f16 v[18:33], v[34:37], v[38:41], v[18:33]
	ds_read_b128 v[34:37], v75
	s_waitcnt lgkmcnt(0)
	v_mfma_f32_32x32x16_f16 v[2:17], v[34:37], v[38:41], v[2:17]
	v_bitop3_b32 v34, v67, v90, 8 bitop3:0x36
	v_lshl_or_b32 v73, v34, 4, v89
	ds_read_b128 v[34:37], v73
	v_add_co_u32_e32 v38, vcc, s0, v68
	s_mov_b32 s0, 0xb000
	s_nop 0
	v_addc_co_u32_e32 v39, vcc, 0, v69, vcc
	s_waitcnt vmcnt(3) lgkmcnt(0)
	v_mfma_f32_32x32x16_f16 v[2:17], v[34:37], v[58:61], v[2:17]
	v_bitop3_b32 v34, v67, v71, 10 bitop3:0x36
	global_load_dwordx4 v[46:49], v[38:39], off offset:-4096
	v_add_co_u32_e32 v86, vcc, s0, v68
	s_mov_b32 s0, 0xd000
	s_nop 0
	v_addc_co_u32_e32 v87, vcc, 0, v69, vcc
	v_mfma_f32_32x32x16_f16 v[18:33], v[54:57], v[58:61], v[18:33]
	v_lshl_or_b32 v58, v34, 4, v88
	ds_read_b128 v[34:37], v58
	v_bitop3_b32 v54, v67, v90, 10 bitop3:0x36
	v_lshl_or_b32 v59, v54, 4, v89
	v_bitop3_b32 v54, v67, v71, 12 bitop3:0x36
	v_lshl_or_b32 v56, v54, 4, v88
	ds_read_b128 v[82:85], v56
	s_waitcnt vmcnt(3) lgkmcnt(1)
	v_mfma_f32_32x32x16_f16 v[18:33], v[34:37], v[42:45], v[18:33]
	ds_read_b128 v[34:37], v59
	v_bitop3_b32 v54, v67, v90, 14 bitop3:0x36
	v_lshl_or_b32 v54, v54, 4, v89
	s_waitcnt lgkmcnt(0)
	v_mfma_f32_32x32x16_f16 v[2:17], v[34:37], v[42:45], v[2:17]
	v_bitop3_b32 v34, v67, v90, 12 bitop3:0x36
	v_lshl_or_b32 v57, v34, 4, v89
	ds_read_b128 v[34:37], v57
	global_load_dwordx4 v[42:45], v[86:87], off offset:-4096
	s_waitcnt vmcnt(3) lgkmcnt(0)
	v_mfma_f32_32x32x16_f16 v[2:17], v[34:37], v[62:65], v[2:17]
	v_bitop3_b32 v34, v67, v71, 14 bitop3:0x36
	v_lshl_or_b32 v55, v34, 4, v88
	global_load_dwordx4 v[34:37], v[86:87], off
	v_mfma_f32_32x32x16_f16 v[18:33], v[82:85], v[62:65], v[18:33]
	ds_read_b128 v[60:63], v55
	v_add_co_u32_e32 v64, vcc, s0, v68
	s_mov_b32 s0, 0xf000
	s_nop 0
	v_addc_co_u32_e32 v65, vcc, 0, v69, vcc
	s_waitcnt vmcnt(3) lgkmcnt(0)
	v_mfma_f32_32x32x16_f16 v[18:33], v[60:63], v[50:53], v[18:33]
	ds_read_b128 v[60:63], v54
	s_waitcnt lgkmcnt(0)
	v_mfma_f32_32x32x16_f16 v[2:17], v[60:63], v[50:53], v[2:17]
	global_load_dwordx4 v[60:63], v[64:65], off offset:-4096
	ds_read_b128 v[50:53], v80 offset:15360
	global_load_dwordx4 v[38:41], v[38:39], off
	s_waitcnt vmcnt(4) lgkmcnt(0)
	v_mfma_f32_32x32x16_f16 v[18:33], v[50:53], v[46:49], v[18:33]
	ds_read_b128 v[50:53], v81 offset:15360
	s_waitcnt lgkmcnt(0)
	v_mfma_f32_32x32x16_f16 v[2:17], v[50:53], v[46:49], v[2:17]
	ds_read_b128 v[46:49], v78 offset:15360
	global_load_dwordx4 v[50:53], v[64:65], off
	v_add_co_u32_e32 v64, vcc, s0, v68
	s_nop 1
	v_addc_co_u32_e32 v65, vcc, 0, v69, vcc
	v_cmp_gt_u32_e32 vcc, 32, v66
	s_waitcnt vmcnt(1) lgkmcnt(0)
	v_mfma_f32_32x32x16_f16 v[18:33], v[46:49], v[38:41], v[18:33]
	ds_read_b128 v[46:49], v79 offset:15360
	s_waitcnt lgkmcnt(0)
	v_mfma_f32_32x32x16_f16 v[2:17], v[46:49], v[38:41], v[2:17]
	ds_read_b128 v[38:41], v77 offset:15360
	global_load_dwordx4 v[46:49], v[64:65], off offset:-4096
	s_waitcnt lgkmcnt(0)
	v_mfma_f32_32x32x16_f16 v[18:33], v[38:41], v[42:45], v[18:33]
	ds_read_b128 v[38:41], v76 offset:15360
	s_waitcnt lgkmcnt(0)
	v_mfma_f32_32x32x16_f16 v[2:17], v[38:41], v[42:45], v[2:17]
	ds_read_b128 v[42:45], v74 offset:15360
	global_load_dwordx4 v[38:41], v[64:65], off
	s_waitcnt lgkmcnt(0)
	v_mfma_f32_32x32x16_f16 v[18:33], v[42:45], v[34:37], v[18:33]
	ds_read_b128 v[42:45], v75 offset:15360
	s_waitcnt lgkmcnt(0)
	v_mfma_f32_32x32x16_f16 v[2:17], v[42:45], v[34:37], v[2:17]
	ds_read_b128 v[34:37], v72 offset:15360
	s_waitcnt lgkmcnt(0)
	v_mfma_f32_32x32x16_f16 v[18:33], v[34:37], v[60:63], v[18:33]
	ds_read_b128 v[34:37], v73 offset:15360
	s_waitcnt lgkmcnt(0)
	v_mfma_f32_32x32x16_f16 v[2:17], v[34:37], v[60:63], v[2:17]
	ds_read_b128 v[34:37], v58 offset:15360
	s_waitcnt vmcnt(2) lgkmcnt(0)
	v_mfma_f32_32x32x16_f16 v[18:33], v[34:37], v[50:53], v[18:33]
	ds_read_b128 v[34:37], v59 offset:15360
	s_waitcnt lgkmcnt(0)
	v_mfma_f32_32x32x16_f16 v[2:17], v[34:37], v[50:53], v[2:17]
	ds_read_b128 v[34:37], v56 offset:15360
	s_waitcnt vmcnt(1) lgkmcnt(0)
	v_mfma_f32_32x32x16_f16 v[18:33], v[34:37], v[46:49], v[18:33]
	ds_read_b128 v[34:37], v57 offset:15360
	s_waitcnt lgkmcnt(0)
	v_mfma_f32_32x32x16_f16 v[2:17], v[34:37], v[46:49], v[2:17]
	ds_read_b128 v[34:37], v55 offset:15360
	s_waitcnt vmcnt(0) lgkmcnt(0)
	v_mfma_f32_32x32x16_f16 v[18:33], v[34:37], v[38:41], v[18:33]
	ds_read_b128 v[34:37], v54 offset:15360
	s_waitcnt lgkmcnt(0)
	s_barrier
	s_nop 8
	v_add_f32_e32 v42, v70, v18
	v_mfma_f32_32x32x16_f16 v[2:17], v[34:37], v[38:41], v[2:17]
	v_lshlrev_b32_e32 v18, 11, v67
	v_or_b32_e32 v43, v1, v18
	v_add_f32_e32 v19, v70, v19
	ds_write2st64_b32 v43, v42, v19 offset1:2
	v_add_f32_e32 v19, v70, v20
	s_nop 6
	v_add_f32_e32 v3, v70, v3
	v_add_f32_e32 v4, v70, v4
	ds_write2st64_b32 v43, v3, v4 offset0:66 offset1:68
	v_add_f32_e32 v3, v70, v21
	ds_write2st64_b32 v43, v19, v3 offset0:4 offset1:6
	v_add_f32_e32 v3, v70, v5
	v_add_f32_e32 v5, v70, v6
	v_add_f32_e32 v4, v70, v22
	ds_write2st64_b32 v43, v3, v5 offset0:70 offset1:80
	v_add_f32_e32 v3, v70, v23
	ds_write2st64_b32 v43, v4, v3 offset0:16 offset1:18
	v_add_f32_e32 v3, v70, v7
	v_add_f32_e32 v5, v70, v8
	v_add_f32_e32 v4, v70, v24
	ds_write2st64_b32 v43, v3, v5 offset0:82 offset1:84
	v_add_f32_e32 v3, v70, v25
	ds_write2st64_b32 v43, v4, v3 offset0:20 offset1:22
	v_add_f32_e32 v3, v70, v9
	v_add_f32_e32 v5, v70, v10
	v_add_f32_e32 v4, v70, v26
	ds_write2st64_b32 v43, v3, v5 offset0:86 offset1:96
	v_add_f32_e32 v3, v70, v27
	ds_write2st64_b32 v43, v4, v3 offset0:32 offset1:34
	v_add_f32_e32 v3, v70, v11
	v_add_f32_e32 v5, v70, v12
	v_add_f32_e32 v4, v70, v28
	ds_write2st64_b32 v43, v3, v5 offset0:98 offset1:100
	v_add_f32_e32 v3, v70, v29
	ds_write2st64_b32 v43, v4, v3 offset0:36 offset1:38
	v_add_f32_e32 v3, v70, v13
	v_add_f32_e32 v2, v70, v2
	ds_write_b32 v43, v3 offset:26112
	v_add_f32_e32 v3, v70, v30
	ds_write2st64_b32 v43, v3, v2 offset0:48 offset1:64
	s_and_saveexec_b64 s[0:1], vcc
	v_add_f32_e32 v2, v70, v14
	ds_write_b32 v1, v2 offset:28672
	s_or_b64 exec, exec, s[0:1]
	v_lshlrev_b32_e32 v3, 2, v67
	v_add_f32_e32 v4, v70, v31
	v_add_u32_e32 v2, v1, v18
	ds_write_b32 v2, v4 offset:12800
	v_or_b32_e32 v4, 57, v3
	v_cmp_gt_u32_e64 s[0:1], 60, v4
	s_and_saveexec_b64 s[4:5], s[0:1]
	v_lshl_or_b32 v4, v4, 9, v1
	v_add_f32_e32 v5, v70, v15
	ds_write_b32 v4, v5
	s_or_b64 exec, exec, s[4:5]
	v_or_b32_e32 v3, 58, v3
	v_add_f32_e32 v4, v70, v32
	v_cmp_gt_u32_e64 s[0:1], 60, v3
	ds_write_b32 v2, v4 offset:13312
	s_and_saveexec_b64 s[4:5], s[0:1]
	v_lshl_or_b32 v3, v3, 9, v1
	v_add_f32_e32 v4, v70, v16
	ds_write_b32 v3, v4
	s_or_b64 exec, exec, s[4:5]
	v_add_f32_e32 v3, v70, v33
	ds_write_b32 v2, v3 offset:13824
	s_and_saveexec_b64 s[0:1], vcc
	v_add_f32_e32 v2, v70, v17
	ds_write_b32 v1, v2 offset:30208
	s_or_b64 exec, exec, s[0:1]
	v_lshlrev_b32_e32 v1, 4, v0
	v_and_b32_e32 v4, 0x1f0, v1
	v_mov_b32_e32 v5, 0
	v_lshrrev_b32_e32 v1, 5, v0
	v_lshl_add_u64 v[2:3], s[2:3], 0, v[4:5]
	v_add_u32_e32 v6, s16, v1
	s_mov_b32 s2, 0x186a0
	v_cmp_gt_i32_e32 vcc, s2, v6
	s_waitcnt lgkmcnt(0)
	s_barrier
	v_lshl_or_b32 v40, v1, 9, v4
	ds_read_b128 v[8:11], v40
	ds_read_b128 v[12:15], v40 offset:4096
	ds_read_b128 v[16:19], v40 offset:8192
	ds_read_b128 v[20:23], v40 offset:12288
	ds_read_b128 v[24:27], v40 offset:16384
	ds_read_b128 v[28:31], v40 offset:20480
	ds_read_b128 v[32:35], v40 offset:24576
	v_add_u32_e32 v41, 56, v1
	v_min_u32_e32 v42, 59, v41
	v_lshl_or_b32 v42, v42, 9, v4
	ds_read_b128 v[36:39], v42
	v_add_u32_e32 v43, s16, v1
	v_mov_b32_e32 v45, 0
	v_mov_b32_e32 v44, v43
	v_cmp_gt_i32_e32 vcc, s2, v44
	s_and_saveexec_b64 s[0:1], vcc
	v_lshlrev_b64 v[46:47], 9, v[44:45]
	v_lshl_add_u64 v[46:47], v[46:47], 0, v[2:3]
	s_waitcnt lgkmcnt(7)
	global_store_dwordx4 v[46:47], v[8:11], off sc1
	s_or_b64 exec, exec, s[0:1]
	v_add_u32_e32 v44, 8, v43
	v_cmp_gt_i32_e32 vcc, s2, v44
	s_and_saveexec_b64 s[0:1], vcc
	v_lshlrev_b64 v[48:49], 9, v[44:45]
	v_lshl_add_u64 v[48:49], v[48:49], 0, v[2:3]
	s_waitcnt lgkmcnt(6)
	global_store_dwordx4 v[48:49], v[12:15], off sc1
	s_or_b64 exec, exec, s[0:1]
	v_add_u32_e32 v44, 16, v43
	v_cmp_gt_i32_e32 vcc, s2, v44
	s_and_saveexec_b64 s[0:1], vcc
	v_lshlrev_b64 v[46:47], 9, v[44:45]
	v_lshl_add_u64 v[46:47], v[46:47], 0, v[2:3]
	s_waitcnt lgkmcnt(5)
	global_store_dwordx4 v[46:47], v[16:19], off sc1
	s_or_b64 exec, exec, s[0:1]
	v_add_u32_e32 v44, 24, v43
	v_cmp_gt_i32_e32 vcc, s2, v44
	s_and_saveexec_b64 s[0:1], vcc
	v_lshlrev_b64 v[48:49], 9, v[44:45]
	v_lshl_add_u64 v[48:49], v[48:49], 0, v[2:3]
	s_waitcnt lgkmcnt(4)
	global_store_dwordx4 v[48:49], v[20:23], off sc1
	s_or_b64 exec, exec, s[0:1]
	v_add_u32_e32 v44, 32, v43
	v_cmp_gt_i32_e32 vcc, s2, v44
	s_and_saveexec_b64 s[0:1], vcc
	v_lshlrev_b64 v[46:47], 9, v[44:45]
	v_lshl_add_u64 v[46:47], v[46:47], 0, v[2:3]
	s_waitcnt lgkmcnt(3)
	global_store_dwordx4 v[46:47], v[24:27], off sc1
	s_or_b64 exec, exec, s[0:1]
	v_add_u32_e32 v44, 40, v43
	v_cmp_gt_i32_e32 vcc, s2, v44
	s_and_saveexec_b64 s[0:1], vcc
	v_lshlrev_b64 v[48:49], 9, v[44:45]
	v_lshl_add_u64 v[48:49], v[48:49], 0, v[2:3]
	s_waitcnt lgkmcnt(2)
	global_store_dwordx4 v[48:49], v[28:31], off sc1
	s_or_b64 exec, exec, s[0:1]
	v_add_u32_e32 v44, 48, v43
	v_cmp_gt_i32_e32 vcc, s2, v44
	s_and_saveexec_b64 s[0:1], vcc
	v_lshlrev_b64 v[46:47], 9, v[44:45]
	v_lshl_add_u64 v[46:47], v[46:47], 0, v[2:3]
	s_waitcnt lgkmcnt(1)
	global_store_dwordx4 v[46:47], v[32:35], off sc1
	s_or_b64 exec, exec, s[0:1]
	v_add_u32_e32 v44, 56, v43
	v_cmp_gt_i32_e32 vcc, s2, v44
	v_cmp_gt_u32_e64 s[4:5], 60, v41
	s_and_b64 vcc, vcc, s[4:5]
	s_and_saveexec_b64 s[0:1], vcc
	v_lshlrev_b64 v[48:49], 9, v[44:45]
	v_lshl_add_u64 v[48:49], v[48:49], 0, v[2:3]
	s_waitcnt lgkmcnt(0)
	global_store_dwordx4 v[48:49], v[36:39], off sc1
	s_or_b64 exec, exec, s[0:1]
